# baseline (speedup 1.0000x reference)
.Lskip_tabld:
	v_readfirstlane_b32 s4, v156
	s_ashr_i32 s27, s4, 7
	s_lshl_b32 s0, s27, 1
	s_ashr_i32 s1, s0, 31
	s_lshl_b64 s[2:3], s[0:1], 13
	s_add_u32 s2, s8, s2
	s_addc_u32 s3, s9, s3
	s_add_u32 s46, s2, 0x18000
	s_addc_u32 s47, s3, 0
	s_add_u32 s44, s2, 0x28000
	s_addc_u32 s45, s3, 0
	v_or_b32_e32 v8, 0x800, v169
	v_lshlrev_b32_e32 v168, 1, v8
	v_cmp_gt_i32_e32 vcc, 16, v156
	v_lshl_add_u32 v166, v156, 2, v165
	s_and_saveexec_b64 s[2:3], vcc
	ds_write_b32 v166, v155
	s_or_b64 exec, exec, s[2:3]
	s_cmp_lt_i32 s22, 0
	s_cbranch_scc0 .Lskip_stage0
	v_lshl_add_u32 v6, v156, 3, v1
	v_cmp_gt_i32_e32 vcc, 64, v156
	s_waitcnt vmcnt(1)
	ds_write_b64 v6, v[4:5]
	s_and_saveexec_b64 s[2:3], vcc
	s_cbranch_execz .LBB1_7
	s_waitcnt vmcnt(0)
	ds_write_b64 v6, v[2:3] offset:2048
.LBB1_7:
	s_or_b64 exec, exec, s[2:3]
	s_waitcnt vmcnt(0) lgkmcnt(0)
	s_barrier
.Lskip_stage0:
	global_load_dwordx4 v[150:153], v168, s[46:47] offset:-4096
	s_ashr_i32 s2, s4, 6
	s_lshl_b32 s3, s2, 3
	s_and_b32 s5, s3, 8
	s_bfe_u32 s26, s2, 0x10001
	s_or_b32 s5, s26, s5
	s_lshl_b32 s26, s2, 9
	s_and_b32 s26, s26, 0x400
	s_lshl_b32 s5, s5, 4
	s_or_b32 s28, s5, s26
	v_lshrrev_b32_e32 v182, 5, v167
	v_bfe_u32 v2, v156, 4, 1
	v_bitop3_b32 v3, v182, v156, 1 bitop3:0x78
	v_lshlrev_b32_e32 v154, 2, v182
	v_xor_b32_e32 v3, v3, v2
	v_bitop3_b32 v4, v154, v156, 4 bitop3:0x78
	v_and_b32_e32 v5, 10, v156
	v_or3_b32 v3, v5, v4, v3
	s_lshl_b32 s5, s2, 4
	v_lshlrev_b32_e32 v3, 4, v3
	global_load_dwordx4 v[146:149], v168, s[46:47] offset:-3072
	s_lshl_b32 s3, s2, 13
	s_and_b32 s29, s5, 16
	v_lshlrev_b32_e32 v170, 8, v182
	v_lshl_or_b32 v171, v2, 10, v3
	s_or_b32 s26, s29, s3
	v_bitop3_b32 v179, v171, s26, v170 bitop3:0x36
	s_or_b32 s5, s26, 0x280
	v_bitop3_b32 v178, v171, s5, v170 bitop3:0x36
	s_or_b32 s30, s3, 0x800
	s_or_b32 s33, s3, 0x1000
	s_or_b32 s29, s29, 64
	s_or_b32 s34, s29, s33
	v_bitop3_b32 v180, v171, s34, v170 bitop3:0x36
	s_or_b32 s29, s3, s29
	s_or_b32 s29, s29, 0x1280
	s_and_b32 s5, s2, 1
	s_lshl_b32 s31, s5, 4
	s_or_b32 s2, s31, s3
	v_bitop3_b32 v173, v171, s2, v170 bitop3:0x36
	global_load_dwordx4 v[142:145], v168, s[46:47] offset:-2048
	v_bitop3_b32 v34, v156, 31, v156 bitop3:0xc
	v_lshrrev_b32_e32 v35, 4, v34
	v_bitop3_b32 v36, v34, v182, 1 bitop3:0x6c
	v_xor_b32_e32 v36, v36, v35
	v_bitop3_b32 v34, v34, v154, 4 bitop3:0x6c
	v_bitop3_b32 v37, v156, 10, 31 bitop3:8
	v_or3_b32 v34, v37, v34, v36
	v_lshlrev_b32_e32 v35, 10, v35
	v_lshlrev_b32_e32 v34, 4, v34
	v_or3_b32 v154, v35, v34, v170
	v_bitop3_b32 v172, s2, v154, v159 bitop3:0x36
	v_bitop3_b32 v176, v171, s29, v170 bitop3:0x36
	s_or_b32 s29, s31, s30
	s_or_b32 s29, s29, 0xa0
	v_bitop3_b32 v175, v171, s29, v170 bitop3:0x36
	s_or_b32 s29, s2, 0xaa0
	s_xor_b32 s29, s29, 0x80
	v_xor_b32_e32 v174, s29, v154
	s_or_b32 s29, s26, 0x18e0
	global_load_dwordx4 v[138:141], v168, s[46:47] offset:-1024
	v_bitop3_b32 v181, v171, s29, v170 bitop3:0x36
	s_or_b32 s29, s26, 0x1a60
	v_bitop3_b32 v177, v171, s29, v170 bitop3:0x36
	s_or_b32 s29, s31, 64
	s_or_b32 s3, s3, s29
	s_mov_b32 s41, s3
	s_or_b32 s29, s29, s33
	s_mov_b32 s40, s29
	s_or_b32 s3, s2, 0x18e0
	s_mov_b32 s42, s3
	s_or_b32 s2, s2, 0x1ae0
	s_xor_b32 s2, s2, 0x80
	s_mov_b32 s43, s2
	s_lshr_b32 s38, s4, 1
	v_and_b32_e32 v26, 31, v167
	v_and_b32_e32 v27, 3, v167
	v_bfe_u32 v28, v167, 3, 1
	v_bfe_u32 v29, v167, 2, 1
	v_lshl_or_b32 v27, v28, 2, v27
	global_load_dwordx4 v[134:137], v168, s[46:47] offset:0
	v_lshl_or_b32 v27, v29, 3, v27
	v_lshlrev_b32_e32 v32, 9, v182
	v_lshl_add_u32 v30, v27, 3, v32
	v_add_u32_e32 v30, 0x10000, v30
	v_lshl_add_u32 v31, v26, 3, v32
	v_add_u32_e32 v31, 0x10400, v31
	v_xor_b32_e32 v28, 31, v26
	v_lshl_add_u32 v28, v28, 3, v32
	v_add_u32_e32 v28, 0x10400, v28
	v_bfe_u32 v29, v167, 4, 1
	v_mul_u32_u24_e32 v29, 0x78, v29
	v_xor_b32_e32 v254, s38, v29
	v_or_b32_e32 v254, 0x10800, v254
	v_and_b32_e32 v33, 16, v167
	v_cmp_eq_u32_e32 vcc, 0, v33
	ds_read2_b64 v[66:69], v30 offset0:0 offset1:32
	ds_read2_b64 v[70:73], v30 offset0:16 offset1:48
	ds_read2_b64 v[198:201], v31 offset0:0 offset1:32
	ds_read2_b64 v[202:205], v28 offset0:0 offset1:32
	global_load_dwordx4 v[126:129], v168, s[46:47] offset:1024
	ds_read2_b64 v[206:209], v254 offset0:0 offset1:16
	ds_read2_b64 v[210:213], v254 offset0:32 offset1:48
	s_waitcnt lgkmcnt(0)
	v_cndmask_b32_e32 v74, v67, v66, vcc
	v_cndmask_b32_e32 v75, v69, v68, vcc
	v_cndmask_b32_e64 v76, v66, -v67, vcc
	v_cndmask_b32_e64 v77, v68, -v69, vcc
	v_cndmask_b32_e32 v78, v71, v70, vcc
	v_cndmask_b32_e32 v79, v73, v72, vcc
	v_cndmask_b32_e64 v80, v70, -v71, vcc
	v_cndmask_b32_e64 v81, v72, -v73, vcc
	v_cvt_pk_f16_f32 v190, v74, v75
	v_cvt_pk_f16_f32 v191, v74, v75
	v_cvt_pk_f16_f32 v192, v76, v77
	v_cvt_pk_f16_f32 v193, v76, v77
	v_cvt_pk_f16_f32 v194, v78, v79
	v_cvt_pk_f16_f32 v195, v78, v79
	v_cvt_pk_f16_f32 v196, v80, v81
	v_cvt_pk_f16_f32 v197, v80, v81
	global_load_dwordx4 v[122:125], v168, s[46:47] offset:2048
	v_mul_f32_e32 v66, v199, v207
	v_mul_f32_e32 v68, v199, v206
	v_mul_f32_e32 v67, v199, v209
	v_mul_f32_e32 v69, v199, v208
	v_fma_f32 v66, v198, v206, -v66
	v_fma_f32 v68, v198, v207, v68
	v_fma_f32 v67, v198, v208, -v67
	v_fma_f32 v69, v198, v209, v69
	v_cvt_pk_f16_f32 v214, v66, v67
	v_cvt_pk_f16_f32 v216, v68, v69
	v_mul_f32_e32 v70, v201, v211
	v_mul_f32_e32 v72, v201, v210
	v_mul_f32_e32 v71, v201, v213
	v_mul_f32_e32 v73, v201, v212
	v_fma_f32 v70, v200, v210, -v70
	v_fma_f32 v72, v200, v211, v72
	v_fma_f32 v71, v200, v212, -v71
	v_fma_f32 v73, v200, v213, v73
	v_cvt_pk_f16_f32 v215, v70, v71
	global_load_dwordx4 v[130:133], v168, s[46:47] offset:3072
	v_cvt_pk_f16_f32 v217, v72, v73
	v_mul_f32_e32 v66, v203, v207
	v_mul_f32_e32 v68, v203, v206
	v_mul_f32_e32 v67, v203, v209
	v_mul_f32_e32 v69, v203, v208
	v_fma_f32 v66, v202, v206, -v66
	v_fma_f32 v68, v202, v207, v68
	v_fma_f32 v67, v202, v208, -v67
	v_fma_f32 v69, v202, v209, v69
	v_cvt_pk_f16_f32 v218, v66, v67
	v_cvt_pk_f16_f32 v220, v68, v69
	v_mul_f32_e32 v70, v205, v211
	v_mul_f32_e32 v72, v205, v210
	v_mul_f32_e32 v71, v205, v213
	v_mul_f32_e32 v73, v205, v212
	v_fma_f32 v70, v204, v210, -v70
	v_fma_f32 v72, v204, v211, v72
	v_fma_f32 v71, v204, v212, -v71
	v_fma_f32 v73, v204, v213, v73
	global_load_dwordx4 v[86:89], v168, s[44:45] offset:-4096
	v_cvt_pk_f16_f32 v219, v70, v71
	v_cvt_pk_f16_f32 v221, v72, v73
	v_xor_b32_e32 v255, 8, v254
	ds_read2_b64 v[206:209], v255 offset0:0 offset1:16
	ds_read2_b64 v[210:213], v255 offset0:32 offset1:48
	v_mfma_f32_32x32x16_f16 v[2:17], v[190:193], v[214:217], 0
	v_mfma_f32_32x32x16_f16 v[18:33], v[194:197], v[218:221], 0
	s_waitcnt lgkmcnt(0)
	v_mul_f32_e32 v66, v199, v207
	v_mul_f32_e32 v68, v199, v206
	v_mul_f32_e32 v67, v199, v209
	v_mul_f32_e32 v69, v199, v208
	v_fma_f32 v66, v198, v206, -v66
	v_fma_f32 v68, v198, v207, v68
	v_fma_f32 v67, v198, v208, -v67
	v_fma_f32 v69, v198, v209, v69
	v_cvt_pk_f16_f32 v214, v66, v67
	v_cvt_pk_f16_f32 v216, v68, v69
	v_mul_f32_e32 v70, v201, v211
	global_load_dwordx4 v[82:85], v168, s[44:45] offset:-3072
	v_mul_f32_e32 v72, v201, v210
	v_mul_f32_e32 v71, v201, v213
	v_mul_f32_e32 v73, v201, v212
	v_fma_f32 v70, v200, v210, -v70
	v_fma_f32 v72, v200, v211, v72
	v_fma_f32 v71, v200, v212, -v71
	v_fma_f32 v73, v200, v213, v73
	v_cvt_pk_f16_f32 v215, v70, v71
	v_cvt_pk_f16_f32 v217, v72, v73
	v_cvt_pk_f16_f32 v2, v2, v3
	v_cvt_pk_f16_f32 v3, v4, v5
	v_cvt_pk_f16_f32 v4, v6, v7
	v_cvt_pk_f16_f32 v5, v8, v9
	v_cvt_pk_f16_f32 v6, v10, v11
	v_cvt_pk_f16_f32 v7, v12, v13
	v_cvt_pk_f16_f32 v8, v14, v15
	v_cvt_pk_f16_f32 v9, v16, v17
	v_cvt_pk_f16_f32 v18, v18, v19
	v_cvt_pk_f16_f32 v19, v20, v21
	v_cvt_pk_f16_f32 v20, v22, v23
	v_cvt_pk_f16_f32 v21, v24, v25
	v_cvt_pk_f16_f32 v22, v26, v27
	v_cvt_pk_f16_f32 v23, v28, v29
	v_cvt_pk_f16_f32 v24, v30, v31
	v_cvt_pk_f16_f32 v25, v32, v33
	s_setprio 1
	s_waitcnt vmcnt(6)
	v_mul_f32_e32 v66, v203, v207
	v_mul_f32_e32 v68, v203, v206
	v_mfma_f32_32x32x16_f16 v[34:49], v[2:5], v[150:153], 0
	v_mul_f32_e32 v67, v203, v209
	v_mul_f32_e32 v69, v203, v208
	v_mfma_f32_32x32x16_f16 v[34:49], v[18:21], v[146:149], v[34:49]
	v_fma_f32 v66, v202, v206, -v66
	v_fma_f32 v68, v202, v207, v68
	v_mfma_f32_32x32x16_f16 v[34:49], v[6:9], v[142:145], v[34:49]
	v_fma_f32 v67, v202, v208, -v67
	v_fma_f32 v69, v202, v209, v69
	v_mfma_f32_32x32x16_f16 v[34:49], v[22:25], v[138:141], v[34:49]
	v_cvt_pk_f16_f32 v218, v66, v67
	v_cvt_pk_f16_f32 v220, v68, v69
	s_waitcnt vmcnt(2)
	v_mul_f32_e32 v70, v205, v211
	v_mul_f32_e32 v72, v205, v210
	v_mfma_f32_32x32x16_f16 v[50:65], v[2:5], v[134:137], 0
	v_mul_f32_e32 v71, v205, v213
	v_mul_f32_e32 v73, v205, v212
	v_mfma_f32_32x32x16_f16 v[50:65], v[18:21], v[126:129], v[50:65]
	v_fma_f32 v70, v204, v210, -v70
	v_fma_f32 v72, v204, v211, v72
	v_mfma_f32_32x32x16_f16 v[50:65], v[6:9], v[122:125], v[50:65]
	v_fma_f32 v71, v204, v212, -v71
	v_fma_f32 v73, v204, v213, v73
	v_mfma_f32_32x32x16_f16 v[50:65], v[22:25], v[130:133], v[50:65]
	v_cvt_pk_f16_f32 v219, v70, v71
	v_cvt_pk_f16_f32 v221, v72, v73
	v_xor_b32_e32 v255, 16, v254
	ds_read2_b64 v[206:209], v255 offset0:0 offset1:16
	ds_read2_b64 v[210:213], v255 offset0:32 offset1:48
	v_mfma_f32_32x32x16_f16 v[2:17], v[190:193], v[214:217], 0
	v_mfma_f32_32x32x16_f16 v[18:33], v[194:197], v[218:221], 0
	v_cvt_pk_f16_f32 v34, v34, v35
	v_cvt_pk_f16_f32 v35, v36, v37
	v_cvt_pk_f16_f32 v36, v38, v39
	v_cvt_pk_f16_f32 v37, v40, v41
	v_cvt_pk_f16_f32 v38, v42, v43
	v_cvt_pk_f16_f32 v39, v44, v45
	v_cvt_pk_f16_f32 v40, v46, v47
	v_cvt_pk_f16_f32 v41, v48, v49
	v_cvt_pk_f16_f32 v50, v50, v51
	v_cvt_pk_f16_f32 v51, v52, v53
	v_cvt_pk_f16_f32 v52, v54, v55
	v_cvt_pk_f16_f32 v53, v56, v57
	v_cvt_pk_f16_f32 v54, v58, v59
	v_cvt_pk_f16_f32 v55, v60, v61
	v_cvt_pk_f16_f32 v56, v62, v63
	v_cvt_pk_f16_f32 v57, v64, v65
	s_waitcnt vmcnt(2)
	v_cvt_pk_f16_f32 v2, v2, v3
	v_cvt_pk_f16_f32 v3, v4, v5
	v_cvt_pk_f16_f32 v4, v6, v7
	v_cvt_pk_f16_f32 v5, v8, v9
	v_mfma_f32_32x32x16_f16 v[90:105], v[34:37], v[222:225], 0
	v_cvt_pk_f16_f32 v6, v10, v11
	v_cvt_pk_f16_f32 v7, v12, v13
	v_cvt_pk_f16_f32 v8, v14, v15
	v_cvt_pk_f16_f32 v9, v16, v17
	v_mfma_f32_32x32x16_f16 v[106:121], v[34:37], v[238:241], 0
	v_cvt_pk_f16_f32 v18, v18, v19
	v_cvt_pk_f16_f32 v19, v20, v21
	v_cvt_pk_f16_f32 v20, v22, v23
	v_cvt_pk_f16_f32 v21, v24, v25
	v_mfma_f32_32x32x16_f16 v[90:105], v[38:41], v[226:229], v[90:105]
	v_cvt_pk_f16_f32 v22, v26, v27
	v_cvt_pk_f16_f32 v23, v28, v29
	v_cvt_pk_f16_f32 v24, v30, v31
	v_cvt_pk_f16_f32 v25, v32, v33
	v_mfma_f32_32x32x16_f16 v[106:121], v[38:41], v[242:245], v[106:121]
	s_waitcnt lgkmcnt(0)
	v_mul_f32_e32 v66, v199, v207
	v_mul_f32_e32 v68, v199, v206
	v_mul_f32_e32 v67, v199, v209
	v_mfma_f32_32x32x16_f16 v[90:105], v[50:53], v[230:233], v[90:105]
	v_mul_f32_e32 v69, v199, v208
	v_fma_f32 v66, v198, v206, -v66
	v_fma_f32 v68, v198, v207, v68
	v_fma_f32 v67, v198, v208, -v67
	v_mfma_f32_32x32x16_f16 v[106:121], v[50:53], v[246:249], v[106:121]
	v_fma_f32 v69, v198, v209, v69
	v_cvt_pk_f16_f32 v214, v66, v67
	v_cvt_pk_f16_f32 v216, v68, v69
	v_mul_f32_e32 v70, v201, v211
	v_mfma_f32_32x32x16_f16 v[90:105], v[54:57], v[234:237], v[90:105]
	v_mul_f32_e32 v72, v201, v210
	v_mul_f32_e32 v71, v201, v213
	v_mul_f32_e32 v73, v201, v212
	v_fma_f32 v70, v200, v210, -v70
	v_mfma_f32_32x32x16_f16 v[106:121], v[54:57], v[250:253], v[106:121]
	v_fma_f32 v72, v200, v211, v72
	v_fma_f32 v71, v200, v212, -v71
	v_fma_f32 v73, v200, v213, v73
	v_cvt_pk_f16_f32 v215, v70, v71
	v_cvt_pk_f16_f32 v217, v72, v73
	v_mfma_f32_32x32x16_f16 v[34:49], v[2:5], v[150:153], 0
	v_mul_f32_e32 v66, v203, v207
	v_mul_f32_e32 v68, v203, v206
	v_mul_f32_e32 v67, v203, v209
	v_mul_f32_e32 v69, v203, v208
	v_fma_f32 v66, v202, v206, -v66
	v_mfma_f32_32x32x16_f16 v[34:49], v[18:21], v[146:149], v[34:49]
	v_fma_f32 v68, v202, v207, v68
	v_fma_f32 v67, v202, v208, -v67
	v_fma_f32 v69, v202, v209, v69
	v_cvt_pk_f16_f32 v218, v66, v67
	v_cvt_pk_f16_f32 v220, v68, v69
	v_mfma_f32_32x32x16_f16 v[34:49], v[6:9], v[142:145], v[34:49]
	v_mul_f32_e32 v70, v205, v211
	v_mul_f32_e32 v72, v205, v210
	v_mul_f32_e32 v71, v205, v213
	v_mul_f32_e32 v73, v205, v212
	v_fma_f32 v70, v204, v210, -v70
	v_mfma_f32_32x32x16_f16 v[34:49], v[22:25], v[138:141], v[34:49]
	v_fma_f32 v72, v204, v211, v72
	v_fma_f32 v71, v204, v212, -v71
	v_fma_f32 v73, v204, v213, v73
	v_cvt_pk_f16_f32 v219, v70, v71
	v_cvt_pk_f16_f32 v221, v72, v73
	v_mfma_f32_32x32x16_f16 v[50:65], v[2:5], v[134:137], 0
	v_cvt_pk_f16_f32 v90, v90, v91
	v_cvt_pk_f16_f32 v91, v92, v93
	v_cvt_pk_f16_f32 v92, v94, v95
	v_cvt_pk_f16_f32 v93, v96, v97
	v_cvt_pk_f16_f32 v94, v98, v99
	v_mfma_f32_32x32x16_f16 v[50:65], v[18:21], v[126:129], v[50:65]
	v_cvt_pk_f16_f32 v95, v100, v101
	v_cvt_pk_f16_f32 v96, v102, v103
	v_cvt_pk_f16_f32 v97, v104, v105
	v_cvt_pk_f16_f32 v106, v106, v107
	v_cvt_pk_f16_f32 v107, v108, v109
	v_mfma_f32_32x32x16_f16 v[50:65], v[6:9], v[122:125], v[50:65]
	v_cvt_pk_f16_f32 v108, v110, v111
	v_cvt_pk_f16_f32 v109, v112, v113
	v_cvt_pk_f16_f32 v110, v114, v115
	v_cvt_pk_f16_f32 v111, v116, v117
	v_cvt_pk_f16_f32 v112, v118, v119
	v_mfma_f32_32x32x16_f16 v[50:65], v[22:25], v[130:133], v[50:65]
	v_cvt_pk_f16_f32 v113, v120, v121
	ds_write_b128 v173, v[90:93]
	ds_write_b128 v172, v[94:97]
	ds_write_b128 v173, v[106:109] offset:32768
	ds_write_b128 v172, v[110:113] offset:32768
	v_xor_b32_e32 v255, 24, v254
	ds_read2_b64 v[206:209], v255 offset0:0 offset1:16
	ds_read2_b64 v[210:213], v255 offset0:32 offset1:48
	v_mfma_f32_32x32x16_f16 v[2:17], v[190:193], v[214:217], 0
	v_mfma_f32_32x32x16_f16 v[18:33], v[194:197], v[218:221], 0
	v_cvt_pk_f16_f32 v34, v34, v35
	v_cvt_pk_f16_f32 v35, v36, v37
	v_cvt_pk_f16_f32 v36, v38, v39
	v_cvt_pk_f16_f32 v37, v40, v41
	v_cvt_pk_f16_f32 v38, v42, v43
	v_cvt_pk_f16_f32 v39, v44, v45
	v_cvt_pk_f16_f32 v40, v46, v47
	v_cvt_pk_f16_f32 v41, v48, v49
	v_cvt_pk_f16_f32 v50, v50, v51
	v_cvt_pk_f16_f32 v51, v52, v53
	v_cvt_pk_f16_f32 v52, v54, v55
	v_cvt_pk_f16_f32 v53, v56, v57
	v_cvt_pk_f16_f32 v54, v58, v59
	v_cvt_pk_f16_f32 v55, v60, v61
	v_cvt_pk_f16_f32 v56, v62, v63
	v_cvt_pk_f16_f32 v57, v64, v65
	v_mfma_f32_32x32x16_f16 v[90:105], v[34:37], v[222:225], 0
	v_cvt_pk_f16_f32 v2, v2, v3
	v_cvt_pk_f16_f32 v3, v4, v5
	v_cvt_pk_f16_f32 v4, v6, v7
	v_cvt_pk_f16_f32 v5, v8, v9
	v_mfma_f32_32x32x16_f16 v[106:121], v[34:37], v[238:241], 0
	v_cvt_pk_f16_f32 v6, v10, v11
	v_cvt_pk_f16_f32 v7, v12, v13
	v_cvt_pk_f16_f32 v8, v14, v15
	v_cvt_pk_f16_f32 v9, v16, v17
	v_cvt_pk_f16_f32 v18, v18, v19
	v_mfma_f32_32x32x16_f16 v[90:105], v[38:41], v[226:229], v[90:105]
	v_cvt_pk_f16_f32 v19, v20, v21
	v_cvt_pk_f16_f32 v20, v22, v23
	v_cvt_pk_f16_f32 v21, v24, v25
	v_cvt_pk_f16_f32 v22, v26, v27
	v_mfma_f32_32x32x16_f16 v[106:121], v[38:41], v[242:245], v[106:121]
	v_cvt_pk_f16_f32 v23, v28, v29
	v_cvt_pk_f16_f32 v24, v30, v31
	v_cvt_pk_f16_f32 v25, v32, v33
	s_waitcnt lgkmcnt(0)
	v_mul_f32_e32 v66, v199, v207
	v_mfma_f32_32x32x16_f16 v[90:105], v[50:53], v[230:233], v[90:105]
	v_mul_f32_e32 v68, v199, v206
	v_mul_f32_e32 v67, v199, v209
	v_mul_f32_e32 v69, v199, v208
	v_fma_f32 v66, v198, v206, -v66
	v_fma_f32 v68, v198, v207, v68
	v_mfma_f32_32x32x16_f16 v[106:121], v[50:53], v[246:249], v[106:121]
	v_fma_f32 v67, v198, v208, -v67
	v_fma_f32 v69, v198, v209, v69
	v_cvt_pk_f16_f32 v214, v66, v67
	v_cvt_pk_f16_f32 v216, v68, v69
	v_mfma_f32_32x32x16_f16 v[90:105], v[54:57], v[234:237], v[90:105]
	v_mul_f32_e32 v70, v201, v211
	v_mul_f32_e32 v72, v201, v210
	v_mul_f32_e32 v71, v201, v213
	v_mul_f32_e32 v73, v201, v212
	v_fma_f32 v70, v200, v210, -v70
	v_mfma_f32_32x32x16_f16 v[106:121], v[54:57], v[250:253], v[106:121]
	v_fma_f32 v72, v200, v211, v72
	v_fma_f32 v71, v200, v212, -v71
	v_fma_f32 v73, v200, v213, v73
	v_cvt_pk_f16_f32 v215, v70, v71
	v_cvt_pk_f16_f32 v217, v72, v73
	v_mfma_f32_32x32x16_f16 v[34:49], v[2:5], v[150:153], 0
	v_mul_f32_e32 v66, v203, v207
	v_mul_f32_e32 v68, v203, v206
	v_mul_f32_e32 v67, v203, v209
	v_mul_f32_e32 v69, v203, v208
	v_fma_f32 v66, v202, v206, -v66
	v_mfma_f32_32x32x16_f16 v[34:49], v[18:21], v[146:149], v[34:49]
	v_fma_f32 v68, v202, v207, v68
	v_fma_f32 v67, v202, v208, -v67
	v_fma_f32 v69, v202, v209, v69
	v_cvt_pk_f16_f32 v218, v66, v67
	v_cvt_pk_f16_f32 v220, v68, v69
	v_mfma_f32_32x32x16_f16 v[34:49], v[6:9], v[142:145], v[34:49]
	v_mul_f32_e32 v70, v205, v211
	v_mul_f32_e32 v72, v205, v210
	v_mul_f32_e32 v71, v205, v213
	v_mul_f32_e32 v73, v205, v212
	v_fma_f32 v70, v204, v210, -v70
	v_mfma_f32_32x32x16_f16 v[34:49], v[22:25], v[138:141], v[34:49]
	v_fma_f32 v72, v204, v211, v72
	v_fma_f32 v71, v204, v212, -v71
	v_fma_f32 v73, v204, v213, v73
	v_cvt_pk_f16_f32 v219, v70, v71
	v_cvt_pk_f16_f32 v221, v72, v73
	v_cvt_pk_f16_f32 v90, v90, v91
	v_mfma_f32_32x32x16_f16 v[50:65], v[2:5], v[134:137], 0
	v_cvt_pk_f16_f32 v91, v92, v93
	v_cvt_pk_f16_f32 v92, v94, v95
	v_cvt_pk_f16_f32 v93, v96, v97
	v_cvt_pk_f16_f32 v94, v98, v99
	v_cvt_pk_f16_f32 v95, v100, v101
	v_mfma_f32_32x32x16_f16 v[50:65], v[18:21], v[126:129], v[50:65]
	v_cvt_pk_f16_f32 v96, v102, v103
	v_cvt_pk_f16_f32 v97, v104, v105
	v_cvt_pk_f16_f32 v106, v106, v107
	v_cvt_pk_f16_f32 v107, v108, v109
	v_cvt_pk_f16_f32 v108, v110, v111
	v_mfma_f32_32x32x16_f16 v[50:65], v[6:9], v[122:125], v[50:65]
	v_cvt_pk_f16_f32 v109, v112, v113
	v_cvt_pk_f16_f32 v110, v114, v115
	v_cvt_pk_f16_f32 v111, v116, v117
	v_cvt_pk_f16_f32 v112, v118, v119
	v_cvt_pk_f16_f32 v113, v120, v121
	v_mfma_f32_32x32x16_f16 v[50:65], v[22:25], v[130:133], v[50:65]
	v_xor_b32_e32 v74, 0x8a0, v173
	v_xor_b32_e32 v75, 0x8a0, v172
	ds_write_b128 v74, v[90:93]
	ds_write_b128 v75, v[94:97]
	ds_write_b128 v74, v[106:109] offset:32768
	ds_write_b128 v75, v[110:113] offset:32768
	s_nop 0
	v_mfma_f32_32x32x16_f16 v[2:17], v[190:193], v[214:217], 0
	v_mfma_f32_32x32x16_f16 v[18:33], v[194:197], v[218:221], 0
	v_cvt_pk_f16_f32 v34, v34, v35
	v_cvt_pk_f16_f32 v35, v36, v37
	v_cvt_pk_f16_f32 v36, v38, v39
	v_cvt_pk_f16_f32 v37, v40, v41
	v_cvt_pk_f16_f32 v38, v42, v43
	v_cvt_pk_f16_f32 v39, v44, v45
	v_cvt_pk_f16_f32 v40, v46, v47
	v_cvt_pk_f16_f32 v41, v48, v49
	v_cvt_pk_f16_f32 v50, v50, v51
	v_cvt_pk_f16_f32 v51, v52, v53
	v_cvt_pk_f16_f32 v52, v54, v55
	v_cvt_pk_f16_f32 v53, v56, v57
	v_cvt_pk_f16_f32 v54, v58, v59
	v_cvt_pk_f16_f32 v55, v60, v61
	v_cvt_pk_f16_f32 v56, v62, v63
	v_cvt_pk_f16_f32 v57, v64, v65
	v_mfma_f32_32x32x16_f16 v[90:105], v[34:37], v[222:225], 0
	v_cvt_pk_f16_f32 v2, v2, v3
	v_cvt_pk_f16_f32 v3, v4, v5
	v_mfma_f32_32x32x16_f16 v[106:121], v[34:37], v[238:241], 0
	v_cvt_pk_f16_f32 v4, v6, v7
	v_cvt_pk_f16_f32 v5, v8, v9
	v_mfma_f32_32x32x16_f16 v[90:105], v[38:41], v[226:229], v[90:105]
	v_cvt_pk_f16_f32 v6, v10, v11
	v_cvt_pk_f16_f32 v7, v12, v13
	v_mfma_f32_32x32x16_f16 v[106:121], v[38:41], v[242:245], v[106:121]
	v_cvt_pk_f16_f32 v8, v14, v15
	v_cvt_pk_f16_f32 v9, v16, v17
	v_mfma_f32_32x32x16_f16 v[90:105], v[50:53], v[230:233], v[90:105]
	v_cvt_pk_f16_f32 v18, v18, v19
	v_cvt_pk_f16_f32 v19, v20, v21
	v_mfma_f32_32x32x16_f16 v[106:121], v[50:53], v[246:249], v[106:121]
	v_cvt_pk_f16_f32 v20, v22, v23
	v_cvt_pk_f16_f32 v21, v24, v25
	v_mfma_f32_32x32x16_f16 v[90:105], v[54:57], v[234:237], v[90:105]
	v_cvt_pk_f16_f32 v22, v26, v27
	v_cvt_pk_f16_f32 v23, v28, v29
	v_mfma_f32_32x32x16_f16 v[106:121], v[54:57], v[250:253], v[106:121]
	v_cvt_pk_f16_f32 v24, v30, v31
	v_cvt_pk_f16_f32 v25, v32, v33
	v_mfma_f32_32x32x16_f16 v[34:49], v[2:5], v[150:153], 0
	v_mfma_f32_32x32x16_f16 v[34:49], v[18:21], v[146:149], v[34:49]
	v_mfma_f32_32x32x16_f16 v[34:49], v[6:9], v[142:145], v[34:49]
	v_mfma_f32_32x32x16_f16 v[34:49], v[22:25], v[138:141], v[34:49]
	v_mfma_f32_32x32x16_f16 v[50:65], v[2:5], v[134:137], 0
	s_nop 5
	v_cvt_pk_f16_f32 v90, v90, v91
	v_cvt_pk_f16_f32 v91, v92, v93
	v_cvt_pk_f16_f32 v92, v94, v95
	v_cvt_pk_f16_f32 v93, v96, v97
	v_mfma_f32_32x32x16_f16 v[50:65], v[18:21], v[126:129], v[50:65]
	v_cvt_pk_f16_f32 v94, v98, v99
	v_cvt_pk_f16_f32 v95, v100, v101
	v_cvt_pk_f16_f32 v96, v102, v103
	v_cvt_pk_f16_f32 v97, v104, v105
	v_cvt_pk_f16_f32 v106, v106, v107
	v_cvt_pk_f16_f32 v107, v108, v109
	v_mfma_f32_32x32x16_f16 v[50:65], v[6:9], v[122:125], v[50:65]
	v_cvt_pk_f16_f32 v108, v110, v111
	v_cvt_pk_f16_f32 v109, v112, v113
	v_cvt_pk_f16_f32 v110, v114, v115
	v_cvt_pk_f16_f32 v111, v116, v117
	v_cvt_pk_f16_f32 v112, v118, v119
	v_cvt_pk_f16_f32 v113, v120, v121
	v_mfma_f32_32x32x16_f16 v[50:65], v[22:25], v[130:133], v[50:65]
	v_xor_b32_e32 v74, 0x1040, v173
	v_xor_b32_e32 v75, 0x1040, v172
	ds_write_b128 v74, v[90:93]
	ds_write_b128 v75, v[94:97]
	ds_write_b128 v74, v[106:109] offset:32768
	ds_write_b128 v75, v[110:113] offset:32768
	s_nop 11
	v_cvt_pk_f16_f32 v34, v34, v35
	v_cvt_pk_f16_f32 v35, v36, v37
	v_cvt_pk_f16_f32 v36, v38, v39
	v_cvt_pk_f16_f32 v37, v40, v41
	v_cvt_pk_f16_f32 v38, v42, v43
	v_cvt_pk_f16_f32 v39, v44, v45
	v_cvt_pk_f16_f32 v40, v46, v47
	v_cvt_pk_f16_f32 v41, v48, v49
	v_cvt_pk_f16_f32 v50, v50, v51
	v_cvt_pk_f16_f32 v51, v52, v53
	v_cvt_pk_f16_f32 v52, v54, v55
	v_cvt_pk_f16_f32 v53, v56, v57
	v_cvt_pk_f16_f32 v54, v58, v59
	v_cvt_pk_f16_f32 v55, v60, v61
	v_cvt_pk_f16_f32 v56, v62, v63
	v_cvt_pk_f16_f32 v57, v64, v65
	v_mfma_f32_32x32x16_f16 v[90:105], v[34:37], v[222:225], 0
	v_mfma_f32_32x32x16_f16 v[106:121], v[34:37], v[238:241], 0
	v_mfma_f32_32x32x16_f16 v[90:105], v[38:41], v[226:229], v[90:105]
	v_mfma_f32_32x32x16_f16 v[106:121], v[38:41], v[242:245], v[106:121]
	v_mfma_f32_32x32x16_f16 v[90:105], v[50:53], v[230:233], v[90:105]
	v_mfma_f32_32x32x16_f16 v[106:121], v[50:53], v[246:249], v[106:121]
	v_mfma_f32_32x32x16_f16 v[90:105], v[54:57], v[234:237], v[90:105]
	v_mfma_f32_32x32x16_f16 v[106:121], v[54:57], v[250:253], v[106:121]
	v_and_b32_e32 v134, 1, v156
	v_bitop3_b32 v132, v171, s40, v170 bitop3:0x36
	v_bitop3_b32 v131, s41, v154, v160 bitop3:0x36
	v_bitop3_b32 v135, v171, s42, v170 bitop3:0x36
	v_xor_b32_e32 v133, s43, v154
	v_and_b32_e32 v130, 4, v156
	s_lshl_b32 s2, s27, 3
	s_lshl_b32 s3, s5, 2
	s_or_b32 s2, s3, s2
	s_ashr_i32 s3, s2, 31
	s_lshl_b64 s[2:3], s[2:3], 13
	s_add_u32 s2, s20, s2
	s_addc_u32 s3, s21, s3
	v_lshlrev_b32_e32 v154, 1, v169
	v_lshl_add_u64 v[2:3], s[2:3], 0, v[154:155]
	v_add_co_u32_e32 v2, vcc, s23, v2
	s_nop 1
	v_addc_co_u32_e32 v3, vcc, 0, v3, vcc
	v_cvt_pk_f16_f32 v90, v90, v91
	v_cvt_pk_f16_f32 v91, v92, v93
	v_cvt_pk_f16_f32 v92, v94, v95
	v_cvt_pk_f16_f32 v93, v96, v97
	v_cvt_pk_f16_f32 v94, v98, v99
	v_cvt_pk_f16_f32 v95, v100, v101
	v_cvt_pk_f16_f32 v96, v102, v103
	v_cvt_pk_f16_f32 v97, v104, v105
	v_cvt_pk_f16_f32 v106, v106, v107
	v_cvt_pk_f16_f32 v107, v108, v109
	v_cvt_pk_f16_f32 v108, v110, v111
	v_cvt_pk_f16_f32 v109, v112, v113
	v_cvt_pk_f16_f32 v110, v114, v115
	v_cvt_pk_f16_f32 v111, v116, v117
	v_cvt_pk_f16_f32 v112, v118, v119
	v_cvt_pk_f16_f32 v113, v120, v121
	v_xor_b32_e32 v74, 0x18e0, v173
	v_xor_b32_e32 v75, 0x18e0, v172
	ds_write_b128 v74, v[90:93]
	ds_write_b128 v75, v[94:97]
	ds_write_b128 v74, v[106:109] offset:32768
	ds_write_b128 v75, v[110:113] offset:32768
	s_setprio 0
	s_waitcnt lgkmcnt(0)
	s_barrier
	global_load_dwordx4 v[62:65], v154, s[2:3]
	global_load_dwordx4 v[46:49], v154, s[2:3] offset:1024
	global_load_dwordx4 v[42:45], v154, s[2:3] offset:2048
	global_load_dwordx4 v[38:41], v154, s[2:3] offset:3072
	global_load_dwordx4 v[54:57], v[2:3], off offset:1024
	global_load_dwordx4 v[50:53], v[2:3], off offset:2048
	v_lshl_add_u64 v[4:5], s[12:13], 0, v[154:155]
	global_load_dwordx4 v[126:129], v154, s[12:13]
	global_load_dwordx4 v[122:125], v154, s[12:13] offset:1024
	global_load_dwordx4 v[118:121], v154, s[12:13] offset:2048
	global_load_dwordx4 v[114:117], v154, s[12:13] offset:3072
	global_load_dwordx4 v[34:37], v168, s[2:3]
	global_load_dwordx4 v[110:113], v168, s[12:13]
	v_add_co_u32_e32 v4, vcc, s23, v4
	s_nop 1
	v_addc_co_u32_e32 v5, vcc, 0, v5, vcc
	global_load_dwordx4 v[58:61], v[2:3], off offset:3072
	global_load_dwordx4 v[106:109], v[4:5], off offset:1024
	global_load_dwordx4 v[94:97], v[4:5], off offset:2048
	global_load_dwordx4 v[90:93], v[4:5], off offset:3072
	v_bfrev_b32_e32 v3, v156
	v_lshlrev_b32_e32 v7, 5, v167
	v_lshlrev_b32_e32 v6, 9, v167
	v_and_b32_e32 v7, 0x200, v7
	v_lshlrev_b32_e32 v8, 8, v167
	v_lshrrev_b32_e32 v3, 27, v3
	v_lshrrev_b32_e32 v2, 2, v167
	v_lshrrev_b32_e32 v4, 4, v156
	v_xor_b32_e32 v5, v169, v156
	v_and_b32_e32 v6, 0x5800, v6
	v_and_b32_e32 v3, 8, v3
	v_and_or_b32 v7, v8, s24, v7
	v_lshrrev_b32_e32 v5, 1, v5
	v_xor_b32_e32 v4, v2, v4
	v_or3_b32 v3, v7, v6, v3
	v_bitop3_b32 v7, v2, v182, 1 bitop3:0x6c
	v_lshlrev_b32_e32 v2, 1, v167
	v_and_b32_e32 v5, 4, v5
	v_lshlrev_b32_e32 v4, 3, v4
	v_lshrrev_b32_e32 v6, 1, v167
	v_and_b32_e32 v2, 2, v2
	v_and_or_b32 v9, v169, 8, v2
	v_and_b32_e32 v2, 8, v4
	v_and_or_b32 v4, v6, 2, v5
	v_or3_b32 v2, v4, v2, v134
	v_lshlrev_b32_e32 v2, 4, v2
	v_bitop3_b32 v146, v3, s28, v2 bitop3:0x36
	v_xor_b32_e32 v8, v6, v182
	v_xor_b32_e32 v147, 0x2010, v146
	v_lshlrev_b32_e32 v8, 2, v8
	v_and_b32_e32 v8, 4, v8
	v_or3_b32 v6, v9, v7, v8
	v_lshlrev_b32_e32 v7, 11, v167
	v_and_b32_e32 v8, 0x7800, v7
	v_lshlrev_b32_e32 v6, 4, v6
	v_or3_b32 v22, v6, v8, v170
	v_and_b32_e32 v23, 0x8000, v7
	v_xor_b32_e32 v150, 16, v146
	v_xad_u32 v70, v22, s28, v23
	v_xor_b32_e32 v151, 0x2000, v146
	ds_read_b64_tr_b16 v[18:19], v146
	ds_read_b64_tr_b16 v[20:21], v147
	ds_read_b64_tr_b16 v[22:23], v146 offset:32768
	ds_read_b64_tr_b16 v[24:25], v147 offset:32768
	ds_read_b64_tr_b16 v[26:27], v150
	ds_read_b64_tr_b16 v[28:29], v151
	ds_read_b64_tr_b16 v[30:31], v150 offset:32768
	ds_read_b64_tr_b16 v[32:33], v151 offset:32768
	v_xor_b32_e32 v148, 32, v146
	v_xor_b32_e32 v149, 0x2030, v146
	v_xor_b32_e32 v144, 48, v146
	v_xor_b32_e32 v145, 0x2020, v146
	v_xor_b32_e32 v142, 64, v146
	v_xor_b32_e32 v143, 0x2050, v146
	v_xor_b32_e32 v140, 0x50, v146
	v_xor_b32_e32 v141, 0x2040, v146
	v_xor_b32_e32 v138, 0x60, v146
	v_xor_b32_e32 v139, 0x2070, v146
	v_xor_b32_e32 v136, 0x70, v146
	v_xor_b32_e32 v137, 0x2060, v146
	v_xor_b32_e32 v71, 0x60, v70
	s_lshl_b64 s[0:1], s[0:1], 13
	s_add_u32 s0, s8, s0
	s_addc_u32 s1, s9, s1
	s_waitcnt vmcnt(17) lgkmcnt(4)
	v_mfma_f32_32x32x16_f16 v[2:17], v[18:21], v[86:89], 0
	s_waitcnt vmcnt(16)
	v_mfma_f32_32x32x16_f16 v[2:17], v[22:25], v[82:85], v[2:17]
	ds_read_b64_tr_b16 v[206:207], v148
	ds_read_b64_tr_b16 v[208:209], v149
	ds_read_b64_tr_b16 v[210:211], v148 offset:32768
	ds_read_b64_tr_b16 v[212:213], v149 offset:32768
	s_waitcnt lgkmcnt(4)
	v_mfma_f32_32x32x16_f16 v[190:205], v[26:29], v[86:89], 0
	v_mfma_f32_32x32x16_f16 v[190:205], v[30:33], v[82:85], v[190:205]
	s_nop 4
	v_cvt_pk_f16_f32 v2, v2, v3
	v_cvt_pk_f16_f32 v3, v4, v5
	v_cvt_pk_f16_f32 v4, v6, v7
	v_cvt_pk_f16_f32 v5, v8, v9
	v_cvt_pk_f16_f32 v6, v10, v11
	v_cvt_pk_f16_f32 v7, v12, v13
	v_cvt_pk_f16_f32 v8, v14, v15
	v_cvt_pk_f16_f32 v9, v16, v17
	v_xor_b32_e32 v73, 0x280, v70
	ds_write_b128 v70, v[2:5]
	ds_write_b128 v73, v[6:9]
	ds_read_b64_tr_b16 v[18:19], v144
	ds_read_b64_tr_b16 v[20:21], v145
	ds_read_b64_tr_b16 v[22:23], v144 offset:32768
	ds_read_b64_tr_b16 v[24:25], v145 offset:32768
	s_waitcnt lgkmcnt(6)
	v_mfma_f32_32x32x16_f16 v[2:17], v[206:209], v[86:89], 0
	v_mfma_f32_32x32x16_f16 v[2:17], v[210:213], v[82:85], v[2:17]
	v_cvt_pk_f16_f32 v190, v190, v191
	v_cvt_pk_f16_f32 v191, v192, v193
	v_cvt_pk_f16_f32 v192, v194, v195
	v_cvt_pk_f16_f32 v193, v196, v197
	v_cvt_pk_f16_f32 v194, v198, v199
	v_cvt_pk_f16_f32 v195, v200, v201
	v_cvt_pk_f16_f32 v196, v202, v203
	v_cvt_pk_f16_f32 v197, v204, v205
	v_xor_b32_e32 v72, 16, v70
	v_xor_b32_e32 v73, 0x290, v70
	ds_write_b128 v72, v[190:193]
	ds_write_b128 v73, v[194:197]
	ds_read_b64_tr_b16 v[26:27], v142
	ds_read_b64_tr_b16 v[28:29], v143
	ds_read_b64_tr_b16 v[30:31], v142 offset:32768
	ds_read_b64_tr_b16 v[32:33], v143 offset:32768
	s_waitcnt lgkmcnt(6)
	v_mfma_f32_32x32x16_f16 v[190:205], v[18:21], v[86:89], 0
	v_mfma_f32_32x32x16_f16 v[190:205], v[22:25], v[82:85], v[190:205]
	v_cvt_pk_f16_f32 v2, v2, v3
	v_cvt_pk_f16_f32 v3, v4, v5
	v_cvt_pk_f16_f32 v4, v6, v7
	v_cvt_pk_f16_f32 v5, v8, v9
	v_cvt_pk_f16_f32 v6, v10, v11
	v_cvt_pk_f16_f32 v7, v12, v13
	v_cvt_pk_f16_f32 v8, v14, v15
	v_cvt_pk_f16_f32 v9, v16, v17
	v_xor_b32_e32 v72, 32, v70
	v_xor_b32_e32 v73, 0x2a0, v70
	ds_write_b128 v72, v[2:5]
	ds_write_b128 v73, v[6:9]
	ds_read_b64_tr_b16 v[206:207], v140
	ds_read_b64_tr_b16 v[208:209], v141
	ds_read_b64_tr_b16 v[210:211], v140 offset:32768
	ds_read_b64_tr_b16 v[212:213], v141 offset:32768
	s_waitcnt lgkmcnt(6)
	v_mfma_f32_32x32x16_f16 v[2:17], v[26:29], v[86:89], 0
	v_mfma_f32_32x32x16_f16 v[2:17], v[30:33], v[82:85], v[2:17]
	v_cvt_pk_f16_f32 v190, v190, v191
	v_cvt_pk_f16_f32 v191, v192, v193
	v_cvt_pk_f16_f32 v192, v194, v195
	v_cvt_pk_f16_f32 v193, v196, v197
	v_cvt_pk_f16_f32 v194, v198, v199
	v_cvt_pk_f16_f32 v195, v200, v201
	v_cvt_pk_f16_f32 v196, v202, v203
	v_cvt_pk_f16_f32 v197, v204, v205
	v_xor_b32_e32 v72, 48, v70
	v_xor_b32_e32 v73, 0x2b0, v70
	ds_write_b128 v72, v[190:193]
	ds_write_b128 v73, v[194:197]
	ds_read_b64_tr_b16 v[18:19], v138
	ds_read_b64_tr_b16 v[20:21], v139
	ds_read_b64_tr_b16 v[22:23], v138 offset:32768
	ds_read_b64_tr_b16 v[24:25], v139 offset:32768
	s_waitcnt lgkmcnt(6)
	v_mfma_f32_32x32x16_f16 v[190:205], v[206:209], v[86:89], 0
	v_mfma_f32_32x32x16_f16 v[190:205], v[210:213], v[82:85], v[190:205]
	v_cvt_pk_f16_f32 v2, v2, v3
	v_cvt_pk_f16_f32 v3, v4, v5
	v_cvt_pk_f16_f32 v4, v6, v7
	v_cvt_pk_f16_f32 v5, v8, v9
	v_cvt_pk_f16_f32 v6, v10, v11
	v_cvt_pk_f16_f32 v7, v12, v13
	v_cvt_pk_f16_f32 v8, v14, v15
	v_cvt_pk_f16_f32 v9, v16, v17
	v_xor_b32_e32 v72, 64, v70
	v_xor_b32_e32 v73, 0x2c0, v70
	ds_write_b128 v72, v[2:5]
	ds_write_b128 v73, v[6:9]
	ds_read_b64_tr_b16 v[26:27], v136
	ds_read_b64_tr_b16 v[28:29], v137
	ds_read_b64_tr_b16 v[30:31], v136 offset:32768
	ds_read_b64_tr_b16 v[32:33], v137 offset:32768
	s_waitcnt lgkmcnt(6)
	v_mfma_f32_32x32x16_f16 v[2:17], v[18:21], v[86:89], 0
	v_mfma_f32_32x32x16_f16 v[2:17], v[22:25], v[82:85], v[2:17]
	v_cvt_pk_f16_f32 v190, v190, v191
	v_cvt_pk_f16_f32 v191, v192, v193
	v_cvt_pk_f16_f32 v192, v194, v195
	v_cvt_pk_f16_f32 v193, v196, v197
	v_cvt_pk_f16_f32 v194, v198, v199
	v_cvt_pk_f16_f32 v195, v200, v201
	v_cvt_pk_f16_f32 v196, v202, v203
	v_cvt_pk_f16_f32 v197, v204, v205
	v_xor_b32_e32 v72, 0x50, v70
	v_xor_b32_e32 v73, 0x2d0, v70
	ds_write_b128 v72, v[190:193]
	ds_write_b128 v73, v[194:197]
	s_waitcnt lgkmcnt(2)
	v_mfma_f32_32x32x16_f16 v[190:205], v[26:29], v[86:89], 0
	v_mfma_f32_32x32x16_f16 v[190:205], v[30:33], v[82:85], v[190:205]
	v_cvt_pk_f16_f32 v2, v2, v3
	v_cvt_pk_f16_f32 v3, v4, v5
	v_cvt_pk_f16_f32 v4, v6, v7
	v_cvt_pk_f16_f32 v5, v8, v9
	v_cvt_pk_f16_f32 v6, v10, v11
	v_cvt_pk_f16_f32 v7, v12, v13
	v_cvt_pk_f16_f32 v8, v14, v15
	v_cvt_pk_f16_f32 v9, v16, v17
	v_xor_b32_e32 v72, 0x60, v70
	v_xor_b32_e32 v73, 0x2e0, v70
	ds_write_b128 v72, v[2:5]
	ds_write_b128 v73, v[6:9]
	v_cvt_pk_f16_f32 v190, v190, v191
	v_cvt_pk_f16_f32 v191, v192, v193
	v_cvt_pk_f16_f32 v192, v194, v195
	v_cvt_pk_f16_f32 v193, v196, v197
	v_cvt_pk_f16_f32 v194, v198, v199
	v_cvt_pk_f16_f32 v195, v200, v201
	v_cvt_pk_f16_f32 v196, v202, v203
	v_cvt_pk_f16_f32 v197, v204, v205
	v_xor_b32_e32 v72, 0x70, v70
	v_xor_b32_e32 v73, 0x2f0, v70
	ds_write_b128 v72, v[190:193]
	ds_write_b128 v73, v[194:197]
	v_lshl_add_u64 v[2:3], s[0:1], 0, v[154:155]
	v_lshl_add_u64 v[4:5], v[2:3], 0, s[18:19]
	v_add_co_u32_e32 v2, vcc, s25, v2
	s_waitcnt lgkmcnt(0)
	s_nop 0
	v_addc_co_u32_e32 v3, vcc, 0, v3, vcc
	s_barrier
	s_nop 0
	s_nop 0
	global_load_dwordx4 v[102:105], v[2:3], off
	global_load_dwordx4 v[98:101], v[4:5], off offset:1024
	s_setprio 1
	s_add_u32 s0, s2, 0x2000
	s_addc_u32 s1, s3, 0
	v_lshl_add_u64 v[2:3], s[0:1], 0, v[154:155]
	v_add_co_u32_e32 v2, vcc, s23, v2
	global_load_dwordx4 v[66:69], v154, s[0:1]
	global_load_dwordx4 v[70:73], v154, s[0:1] offset:1024
	global_load_dwordx4 v[74:77], v154, s[0:1] offset:2048
	global_load_dwordx4 v[78:81], v154, s[0:1] offset:3072
	v_addc_co_u32_e32 v3, vcc, 0, v3, vcc
	global_load_dwordx4 v[82:85], v168, s[0:1]
	global_load_dwordx4 v[86:89], v[2:3], off offset:1024
	global_load_dwordx4 v[182:185], v[2:3], off offset:2048
	global_load_dwordx4 v[186:189], v[2:3], off offset:3072
	ds_read_b128 v[18:21], v179
	ds_read_b128 v[22:25], v179 offset:32768
	ds_read_b128 v[26:29], v178
	ds_read_b128 v[30:33], v178 offset:32768
	s_add_u32 s0, s2, 0x6000
	s_addc_u32 s1, s3, 0
	s_waitcnt vmcnt(25) lgkmcnt(3)
	v_mfma_f32_32x32x16_f16 v[2:17], v[18:21], v[62:65], 0
	s_add_u32 s2, s2, 0x4000
	s_addc_u32 s3, s3, 0
	s_or_b32 s27, s26, 0x8a0
	s_or_b32 s26, s26, 0xa20
	s_waitcnt vmcnt(24) lgkmcnt(1)
	v_mfma_f32_32x32x16_f16 v[2:17], v[26:29], v[46:49], v[2:17]
	s_waitcnt vmcnt(23)
	v_mfma_f32_32x32x16_f16 v[2:17], v[22:25], v[42:45], v[2:17]
	s_waitcnt vmcnt(22) lgkmcnt(0)
	v_mfma_f32_32x32x16_f16 v[2:17], v[30:33], v[38:41], v[2:17]
	s_waitcnt vmcnt(15)
	v_mfma_f32_32x32x16_f16 v[34:49], v[18:21], v[34:37], 0
	s_nop 9
	v_cvt_pk_f16_f32 v9, v8, v9
	v_cvt_pk_f16_f32 v8, v6, v7
	v_cvt_pk_f16_f32 v7, v4, v5
	v_cvt_pk_f16_f32 v6, v2, v3
	v_cvt_pk_f16_f32 v5, v16, v17
	v_cvt_pk_f16_f32 v4, v14, v15
	v_cvt_pk_f16_f32 v3, v12, v13
	v_mfma_f32_32x32x16_f16 v[34:49], v[26:29], v[54:57], v[34:49]
	v_cvt_pk_f16_f32 v2, v10, v11
	v_mfma_f32_32x32x16_f16 v[34:49], v[22:25], v[50:53], v[34:49]
	s_waitcnt vmcnt(13)
	v_mfma_f32_32x32x16_f16 v[34:49], v[30:33], v[58:61], v[34:49]
	v_mfma_f32_32x32x16_f16 v[18:33], v[6:9], v[126:129], 0
	s_nop 10
	v_cvt_pk_f16_f32 v13, v40, v41
	v_cvt_pk_f16_f32 v12, v38, v39
	v_cvt_pk_f16_f32 v11, v36, v37
	v_cvt_pk_f16_f32 v10, v34, v35
	v_cvt_pk_f16_f32 v17, v48, v49
	v_cvt_pk_f16_f32 v16, v46, v47
	v_cvt_pk_f16_f32 v15, v44, v45
	v_mfma_f32_32x32x16_f16 v[50:65], v[6:9], v[110:113], 0
	v_bitop3_b32 v6, v171, s27, v170 bitop3:0x36
	v_cvt_pk_f16_f32 v14, v42, v43
	v_mfma_f32_32x32x16_f16 v[18:33], v[2:5], v[122:125], v[18:33]
	s_waitcnt vmcnt(12)
	v_mfma_f32_32x32x16_f16 v[50:65], v[2:5], v[106:109], v[50:65]
	ds_read_b128 v[2:5], v6
	ds_read_b128 v[6:9], v6 offset:32768
	v_mfma_f32_32x32x16_f16 v[18:33], v[10:13], v[118:121], v[18:33]
	s_waitcnt vmcnt(11)
	v_mfma_f32_32x32x16_f16 v[50:65], v[10:13], v[94:97], v[50:65]
	s_waitcnt vmcnt(7) lgkmcnt(1)
	v_mfma_f32_32x32x16_f16 v[34:49], v[2:5], v[66:69], 0
	v_mfma_f32_32x32x16_f16 v[18:33], v[14:17], v[114:117], v[18:33]
	v_mfma_f32_32x32x16_f16 v[50:65], v[14:17], v[90:93], v[50:65]
	v_bitop3_b32 v14, v171, s26, v170 bitop3:0x36
	ds_read_b128 v[10:13], v14
	ds_read_b128 v[14:17], v14 offset:32768
	s_nop 7
	v_cvt_pk_f16_f32 v25, v24, v25
	v_cvt_pk_f16_f32 v24, v22, v23
	v_cvt_pk_f16_f32 v23, v20, v21
	v_cvt_pk_f16_f32 v22, v18, v19
	v_cvt_pk_f16_f32 v21, v32, v33
	s_waitcnt vmcnt(6) lgkmcnt(1)
	v_mfma_f32_32x32x16_f16 v[34:49], v[10:13], v[70:73], v[34:49]
	v_cvt_pk_f16_f32 v20, v30, v31
	v_cvt_pk_f16_f32 v19, v28, v29
	v_cvt_pk_f16_f32 v18, v26, v27
	ds_write_b128 v173, v[22:25]
	ds_write_b128 v172, v[18:21]
	v_cvt_pk_f16_f32 v21, v56, v57
	v_cvt_pk_f16_f32 v20, v54, v55
	s_waitcnt vmcnt(5)
	v_mfma_f32_32x32x16_f16 v[34:49], v[6:9], v[74:77], v[34:49]
	v_cvt_pk_f16_f32 v19, v52, v53
	v_cvt_pk_f16_f32 v18, v50, v51
	ds_write_b128 v173, v[18:21] offset:32768
	v_cvt_pk_f16_f32 v21, v64, v65
	v_cvt_pk_f16_f32 v20, v62, v63
	v_cvt_pk_f16_f32 v19, v60, v61
	v_cvt_pk_f16_f32 v18, v58, v59
	s_waitcnt vmcnt(4) lgkmcnt(3)
	v_mfma_f32_32x32x16_f16 v[34:49], v[14:17], v[78:81], v[34:49]
	ds_write_b128 v172, v[18:21] offset:32768
	s_waitcnt vmcnt(3)
	v_mfma_f32_32x32x16_f16 v[66:81], v[2:5], v[82:85], 0
	s_nop 8
	v_cvt_pk_f16_f32 v41, v40, v41
	v_cvt_pk_f16_f32 v40, v38, v39
	v_cvt_pk_f16_f32 v39, v36, v37
	v_cvt_pk_f16_f32 v38, v34, v35
	v_cvt_pk_f16_f32 v85, v48, v49
	v_cvt_pk_f16_f32 v84, v46, v47
	v_cvt_pk_f16_f32 v83, v44, v45
	s_waitcnt vmcnt(2)
	v_mfma_f32_32x32x16_f16 v[66:81], v[10:13], v[86:89], v[66:81]
	v_cvt_pk_f16_f32 v82, v42, v43
	s_waitcnt vmcnt(1)
	v_mfma_f32_32x32x16_f16 v[66:81], v[6:9], v[182:185], v[66:81]
	s_waitcnt vmcnt(0)
	v_mfma_f32_32x32x16_f16 v[66:81], v[14:17], v[186:189], v[66:81]
	v_mfma_f32_32x32x16_f16 v[2:17], v[38:41], v[126:129], 0
	s_nop 10
	v_cvt_pk_f16_f32 v73, v72, v73
	v_cvt_pk_f16_f32 v72, v70, v71
	v_cvt_pk_f16_f32 v70, v66, v67
	v_cvt_pk_f16_f32 v67, v76, v77
	v_cvt_pk_f16_f32 v66, v74, v75
	global_load_dwordx4 v[74:77], v154, s[2:3]
	v_cvt_pk_f16_f32 v71, v68, v69
	v_cvt_pk_f16_f32 v69, v80, v81
	v_cvt_pk_f16_f32 v68, v78, v79
	global_load_dwordx4 v[78:81], v154, s[2:3] offset:1024
	ds_read_b128 v[18:21], v180
	ds_read_b128 v[22:25], v176
	ds_read_b128 v[26:29], v180 offset:32768
	global_load_dwordx4 v[30:33], v154, s[2:3] offset:2048
	v_mfma_f32_32x32x16_f16 v[34:49], v[38:41], v[110:113], 0
	v_mfma_f32_32x32x16_f16 v[2:17], v[82:85], v[122:125], v[2:17]
	v_mfma_f32_32x32x16_f16 v[34:49], v[82:85], v[106:109], v[34:49]
	ds_read_b128 v[82:85], v176 offset:32768
	s_waitcnt vmcnt(2) lgkmcnt(3)
	v_mfma_f32_32x32x16_f16 v[50:65], v[18:21], v[74:77], 0
	v_mfma_f32_32x32x16_f16 v[2:17], v[70:73], v[118:121], v[2:17]
	v_mfma_f32_32x32x16_f16 v[34:49], v[70:73], v[94:97], v[34:49]
	v_lshl_add_u64 v[70:71], s[2:3], 0, v[154:155]
	v_add_co_u32_e32 v152, vcc, s23, v70
	s_nop 1
	v_addc_co_u32_e32 v153, vcc, 0, v71, vcc
	s_waitcnt vmcnt(1) lgkmcnt(2)
	v_mfma_f32_32x32x16_f16 v[50:65], v[22:25], v[78:81], v[50:65]
	v_mfma_f32_32x32x16_f16 v[2:17], v[66:69], v[114:117], v[2:17]
	v_mfma_f32_32x32x16_f16 v[34:49], v[66:69], v[90:93], v[34:49]
	global_load_dwordx4 v[66:69], v154, s[2:3] offset:3072
	s_nop 9
	v_cvt_pk_f16_f32 v9, v8, v9
	v_cvt_pk_f16_f32 v8, v6, v7
	v_cvt_pk_f16_f32 v7, v4, v5
	v_cvt_pk_f16_f32 v6, v2, v3
	v_cvt_pk_f16_f32 v5, v16, v17
	v_cvt_pk_f16_f32 v4, v14, v15
	s_waitcnt vmcnt(1) lgkmcnt(1)
	v_mfma_f32_32x32x16_f16 v[50:65], v[26:29], v[30:33], v[50:65]
	global_load_dwordx4 v[30:33], v168, s[2:3]
	global_load_dwordx4 v[86:89], v[152:153], off offset:1024
	s_nop 0
	global_load_dwordx4 v[168:171], v168, s[0:1]
	v_cvt_pk_f16_f32 v3, v12, v13
	v_cvt_pk_f16_f32 v2, v10, v11
	ds_write_b128 v175, v[6:9]
	ds_write_b128 v174, v[2:5]
	v_cvt_pk_f16_f32 v5, v40, v41
	s_waitcnt vmcnt(3) lgkmcnt(2)
	v_mfma_f32_32x32x16_f16 v[50:65], v[82:85], v[66:69], v[50:65]
	global_load_dwordx4 v[182:185], v154, s[0:1] offset:1024
	v_cvt_pk_f16_f32 v4, v38, v39
	v_cvt_pk_f16_f32 v3, v36, v37
	v_cvt_pk_f16_f32 v2, v34, v35
	ds_write_b128 v175, v[2:5] offset:32768
	v_cvt_pk_f16_f32 v5, v48, v49
	v_cvt_pk_f16_f32 v4, v46, v47
	s_waitcnt vmcnt(3)
	v_mfma_f32_32x32x16_f16 v[66:81], v[18:21], v[30:33], 0
	global_load_dwordx4 v[18:21], v[152:153], off offset:2048
	v_cvt_pk_f16_f32 v3, v44, v45
	v_cvt_pk_f16_f32 v2, v42, v43
	ds_write_b128 v174, v[2:5] offset:32768
	v_cvt_pk_f16_f32 v57, v56, v57
	v_cvt_pk_f16_f32 v56, v54, v55
	v_cvt_pk_f16_f32 v55, v52, v53
	s_waitcnt vmcnt(3)
	v_mfma_f32_32x32x16_f16 v[66:81], v[22:25], v[86:89], v[66:81]
	global_load_dwordx4 v[22:25], v[152:153], off offset:3072
	v_cvt_pk_f16_f32 v54, v50, v51
	s_waitcnt vmcnt(1)
	v_mfma_f32_32x32x16_f16 v[66:81], v[26:29], v[18:21], v[66:81]
	v_lshl_add_u64 v[18:19], s[0:1], 0, v[154:155]
	v_add_co_u32_e32 v152, vcc, s23, v18
	s_nop 1
	v_addc_co_u32_e32 v153, vcc, 0, v19, vcc
	global_load_dwordx4 v[86:89], v[152:153], off offset:1024
	s_waitcnt vmcnt(1)
	v_mfma_f32_32x32x16_f16 v[66:81], v[82:85], v[22:25], v[66:81]
	v_cvt_pk_f16_f32 v85, v64, v65
	v_cvt_pk_f16_f32 v84, v62, v63
	v_cvt_pk_f16_f32 v83, v60, v61
	v_cvt_pk_f16_f32 v82, v58, v59
	v_mfma_f32_32x32x16_f16 v[18:33], v[54:57], v[126:129], 0
	s_nop 6
	v_cvt_pk_f16_f32 v73, v72, v73
	v_cvt_pk_f16_f32 v72, v70, v71
	v_cvt_pk_f16_f32 v70, v66, v67
	v_cvt_pk_f16_f32 v67, v76, v77
	v_cvt_pk_f16_f32 v66, v74, v75
	global_load_dwordx4 v[74:77], v154, s[0:1]
	ds_read_b128 v[2:5], v181
	ds_read_b128 v[6:9], v177
	ds_read_b128 v[10:13], v181 offset:32768
	global_load_dwordx4 v[14:17], v154, s[0:1] offset:2048
	global_load_dwordx4 v[34:37], v154, s[0:1] offset:3072
	v_mfma_f32_32x32x16_f16 v[50:65], v[54:57], v[110:113], 0
	v_cvt_pk_f16_f32 v71, v68, v69
	v_cvt_pk_f16_f32 v69, v80, v81
	v_cvt_pk_f16_f32 v68, v78, v79
	v_mfma_f32_32x32x16_f16 v[18:33], v[82:85], v[122:125], v[18:33]
	v_mfma_f32_32x32x16_f16 v[50:65], v[82:85], v[106:109], v[50:65]
	ds_read_b128 v[82:85], v177 offset:32768
	v_mfma_f32_32x32x16_f16 v[18:33], v[70:73], v[118:121], v[18:33]
	v_mfma_f32_32x32x16_f16 v[50:65], v[70:73], v[94:97], v[50:65]
	v_mfma_f32_32x32x16_f16 v[18:33], v[66:69], v[114:117], v[18:33]
	v_mfma_f32_32x32x16_f16 v[50:65], v[66:69], v[90:93], v[50:65]
	s_nop 10
	v_cvt_pk_f16_f32 v25, v24, v25
	v_cvt_pk_f16_f32 v24, v22, v23
	v_cvt_pk_f16_f32 v23, v20, v21
	v_cvt_pk_f16_f32 v22, v18, v19
	ds_write_b128 v132, v[22:25]
	s_waitcnt vmcnt(2) lgkmcnt(4)
	v_mfma_f32_32x32x16_f16 v[66:81], v[2:5], v[74:77], 0
	s_waitcnt lgkmcnt(3)
	v_mfma_f32_32x32x16_f16 v[66:81], v[6:9], v[182:185], v[66:81]
	s_waitcnt vmcnt(1) lgkmcnt(2)
	v_mfma_f32_32x32x16_f16 v[66:81], v[10:13], v[14:17], v[66:81]
	s_waitcnt vmcnt(0) lgkmcnt(1)
	v_mfma_f32_32x32x16_f16 v[66:81], v[82:85], v[34:37], v[66:81]
	v_mfma_f32_32x32x16_f16 v[34:49], v[2:5], v[168:171], 0
	global_load_dwordx4 v[2:5], v[152:153], off offset:2048
	s_nop 9
	v_cvt_pk_f16_f32 v73, v72, v73
	v_cvt_pk_f16_f32 v72, v70, v71
	v_cvt_pk_f16_f32 v71, v68, v69
	v_cvt_pk_f16_f32 v70, v66, v67
	v_cvt_pk_f16_f32 v69, v80, v81
	v_cvt_pk_f16_f32 v68, v78, v79
	v_mfma_f32_32x32x16_f16 v[34:49], v[6:9], v[86:89], v[34:49]
	global_load_dwordx4 v[6:9], v[152:153], off offset:3072
	v_cvt_pk_f16_f32 v67, v76, v77
	v_cvt_pk_f16_f32 v66, v74, v75
	s_waitcnt vmcnt(1)
	v_mfma_f32_32x32x16_f16 v[34:49], v[10:13], v[2:5], v[34:49]
	s_waitcnt vmcnt(0)
	v_mfma_f32_32x32x16_f16 v[34:49], v[82:85], v[6:9], v[34:49]
	v_mfma_f32_32x32x16_f16 v[2:17], v[70:73], v[126:129], 0
	s_nop 10
	v_cvt_pk_f16_f32 v41, v40, v41
	v_cvt_pk_f16_f32 v40, v38, v39
	v_cvt_pk_f16_f32 v38, v34, v35
	v_cvt_pk_f16_f32 v35, v44, v45
	v_cvt_pk_f16_f32 v34, v42, v43
	v_cvt_pk_f16_f32 v45, v32, v33
	v_cvt_pk_f16_f32 v44, v30, v31
	v_cvt_pk_f16_f32 v43, v28, v29
	v_cvt_pk_f16_f32 v42, v26, v27
	v_mfma_f32_32x32x16_f16 v[18:33], v[70:73], v[110:113], 0
	v_cvt_pk_f16_f32 v39, v36, v37
	v_cvt_pk_f16_f32 v37, v48, v49
	v_cvt_pk_f16_f32 v36, v46, v47
	ds_write_b128 v131, v[42:45]
	v_cvt_pk_f16_f32 v45, v56, v57
	v_cvt_pk_f16_f32 v44, v54, v55
	v_cvt_pk_f16_f32 v43, v52, v53
	v_mfma_f32_32x32x16_f16 v[2:17], v[66:69], v[122:125], v[2:17]
	v_cvt_pk_f16_f32 v42, v50, v51
	ds_write_b128 v132, v[42:45] offset:32768
	v_cvt_pk_f16_f32 v45, v64, v65
	v_cvt_pk_f16_f32 v44, v62, v63
	v_cvt_pk_f16_f32 v43, v60, v61
	v_cvt_pk_f16_f32 v42, v58, v59
	ds_write_b128 v131, v[42:45] offset:32768
	v_mfma_f32_32x32x16_f16 v[18:33], v[66:69], v[106:109], v[18:33]
	v_mfma_f32_32x32x16_f16 v[2:17], v[38:41], v[118:121], v[2:17]
	v_mfma_f32_32x32x16_f16 v[18:33], v[38:41], v[94:97], v[18:33]
	v_mfma_f32_32x32x16_f16 v[2:17], v[34:37], v[114:117], v[2:17]
	v_mfma_f32_32x32x16_f16 v[18:33], v[34:37], v[90:93], v[18:33]
	s_nop 10
	v_cvt_pk_f16_f32 v9, v8, v9
	v_cvt_pk_f16_f32 v8, v6, v7
	v_cvt_pk_f16_f32 v7, v4, v5
	v_cvt_pk_f16_f32 v6, v2, v3
	v_cvt_pk_f16_f32 v5, v16, v17
	v_cvt_pk_f16_f32 v4, v14, v15
	v_cvt_pk_f16_f32 v3, v12, v13
	v_cvt_pk_f16_f32 v2, v10, v11
	ds_write_b128 v135, v[6:9]
	ds_write_b128 v133, v[2:5]
	v_cvt_pk_f16_f32 v5, v24, v25
	v_cvt_pk_f16_f32 v4, v22, v23
	v_cvt_pk_f16_f32 v3, v20, v21
	v_cvt_pk_f16_f32 v2, v18, v19
	ds_write_b128 v135, v[2:5] offset:32768
	v_cvt_pk_f16_f32 v5, v32, v33
	v_cvt_pk_f16_f32 v4, v30, v31
	v_cvt_pk_f16_f32 v3, v28, v29
	v_cvt_pk_f16_f32 v2, v26, v27
	ds_write_b128 v133, v[2:5] offset:32768
	s_setprio 0
	s_waitcnt lgkmcnt(0)
	s_barrier
	s_cmp_lt_i32 s22, 0
	s_cbranch_scc0 .Lno_pref
	s_add_u32 s36, s10, 0x140000
	s_addc_u32 s37, s11, 0
	v_lshlrev_b32_e32 v192, 3, v156
	v_lshlrev_b32_e32 v193, 3, v167
	global_load_dwordx2 v[190:191], v192, s[36:37]
	global_load_dwordx2 v[194:195], v193, s[36:37] offset:2048
